# NSA tile loop: max3 row-max tree, permlane32_swap cross-half max, tile-list entry prefetched before the barrier
# baseline (speedup 1.0000x reference)
; __device__ __forceinline__ int crow(int r, int hi) { return (r & 3) + 8 * (r >> 2) + 4 * hi; }
; __device__ __forceinline__ void unit(LAS unsigned char* lds, const bf16* Z, const bf16* kct, const bf16* vct, bf16* OAp, int b, int g, int iq, const int tid_in) {
;     ...
;         float mref = 0.f, l_run = 0.f; f32x16 o[2];
; #pragma unroll
;         for (int r = 0; r < 16; ++r) { o[0][r] = 0.f; o[1][r] = 0.f; }
;         int curbr = TL[1] >> 8; bool first = true;
;         for (int k = 0; k < ntile; ++k) {
;             const int e = TL[1 + k], n = e & 0xff, br = e >> 8, bi = k & 1;
;             if (br != curbr) {
;                 l_run += __shfl_xor(l_run, 32);
;                 const float sc = gate[1] / l_run;
; #pragma unroll
;                 for (int r = 0; r < 16; ++r) { otot[0][r] += sc * o[0][r]; otot[1][r] += sc * o[1][r]; o[0][r] = 0.f; o[1][r] = 0.f; }
;                 mref = 0.f; l_run = 0.f; curbr = br; first = true;
;             }
;             const bool sel = (br == 1) ? (((mymask >> n) & 1u) != 0u) : true;
;             const float base = sel ? (slope2 * (float)(64 * n + 4 * hi - t) - mref) : -INFINITY;
;             f32x16 p0, p1;
;             if (n == iq) {
; #pragma unroll
;                 for (int r = 0; r < 16; ++r) { const float cr = (float)((r & 3) + 8 * (r >> 2)); const int c = crow(r, hi);
;                     p0[r] = (c > tl) ? -INFINITY : fmaf(slope2, cr, base); p1[r] = (c + 32 > tl) ? -INFINITY : fmaf(slope2, cr + 32.f, base); }
.LBB0_484:
	v_add_f32_e32 v35, v35, v51
	v_add_f32_e32 v51, v73, v74
	v_add_f32_e32 v35, 0, v35
	v_add_f32_e32 v62, v77, v78
	v_add_f32_e32 v35, v51, v35
	v_add_f32_e32 v63, v79, v80
	v_add_f32_e32 v35, v62, v35
	v_pk_add_f32 v[36:37], v[36:37], v[38:39]
	v_add_f32_e32 v35, v63, v35
	v_add_f32_e32 v35, v37, v35
	v_pk_add_f32 v[38:39], v[40:41], v[42:43]
	v_add_f32_e32 v35, v36, v35
	v_add_f32_e32 v35, v39, v35
	v_pk_add_f32 v[40:41], v[44:45], v[46:47]
	v_add_f32_e32 v35, v38, v35
	v_add_f32_e32 v35, v41, v35
	v_pk_add_f32 v[42:43], v[48:49], v[52:53]
	v_add_f32_e32 v35, v40, v35
	v_add_f32_e32 v35, v43, v35
	v_pk_add_f32 v[44:45], v[54:55], v[56:57]
	v_add_f32_e32 v35, v42, v35
	v_add_f32_e32 v35, v45, v35
	v_pk_add_f32 v[46:47], v[58:59], v[60:61]
	v_add_f32_e32 v35, v44, v35
	v_add_f32_e32 v35, v47, v35
	s_waitcnt lgkmcnt(0)
	s_barrier
	v_add_f32_e32 v35, v46, v35
	v_pk_add_f32 v[166:167], v[34:35], 0 op_sel_hi:[1,0]
	s_cmp_eq_u32 s19, 1
	s_cbranch_scc1 .LBB0_411
	v_cmp_gt_u32_e64 s[42:43], v1, v68
	v_or_b32_e32 v1, 35, v122
	v_cmp_gt_u32_e64 s[44:45], v1, v68
	v_or_b32_e32 v1, 40, v122
	v_cmp_gt_u32_e64 s[48:49], v1, v68
	v_or_b32_e32 v1, 41, v122
	v_cmp_gt_u32_e64 s[52:53], v1, v68
	v_or_b32_e32 v1, 10, v122
	v_cmp_gt_u32_e64 s[54:55], v1, v68
	v_or_b32_e32 v1, 42, v122
	v_cmp_gt_u32_e64 s[56:57], v1, v68
	v_or_b32_e32 v1, 11, v122
	v_cmp_gt_u32_e64 s[58:59], v1, v68
	v_or_b32_e32 v1, 43, v122
	v_cmp_gt_u32_e64 s[60:61], v1, v68
	v_or_b32_e32 v1, 48, v122
	v_cmp_gt_u32_e64 s[64:65], v1, v68
	v_or_b32_e32 v1, 49, v122
	v_and_b32_e32 v34, 0xffff0000, v69
	v_cmp_gt_u32_e64 s[68:69], v1, v68
	v_or_b32_e32 v1, 18, v122
	v_mul_f32_e32 v34, 0xbfb8aa3b, v34
	v_cmp_gt_u32_e64 s[70:71], v1, v68
	v_or_b32_e32 v1, 50, v122
	v_exp_f32_e32 v34, v34
	v_cmp_gt_u32_e64 s[72:73], v1, v68
	v_or_b32_e32 v1, 19, v122
	v_cmp_gt_u32_e64 s[74:75], v1, v68
	v_or_b32_e32 v1, 51, v122
	v_cmp_gt_u32_e64 s[76:77], v1, v68
	v_or_b32_e32 v1, 56, v122
	v_cmp_gt_u32_e64 s[80:81], v1, v68
	v_or_b32_e32 v1, 57, v122
	v_add_f32_e32 v34, 1.0, v34
	v_cmp_gt_u32_e64 s[84:85], v1, v68
	v_or_b32_e32 v1, 26, v122
	v_rcp_f32_e32 v181, v34
	v_cmp_gt_u32_e64 s[86:87], v1, v68
	v_or_b32_e32 v1, 58, v122
	v_cmp_gt_u32_e64 s[88:89], v1, v68
	v_or_b32_e32 v1, 27, v122
	v_or_b32_e32 v34, 34, v122
	v_cmp_gt_u32_e64 s[90:91], v1, v68
	v_or_b32_e32 v1, 59, v122
	v_cmp_gt_u32_e64 s[0:1], v122, v68
	v_cmp_gt_u32_e64 s[4:5], v75, v68
	v_cmp_lt_u32_e64 s[6:7], v122, v68
	v_cmp_gt_u32_e64 s[8:9], v67, v68
	v_cmp_gt_u32_e64 s[38:39], v50, v68
	v_cmp_gt_u32_e64 s[40:41], v34, v68
	v_cmp_gt_u32_e64 s[46:47], v70, v68
	v_cmp_gt_u32_e64 s[50:51], v66, v68
	v_cmp_gt_u32_e64 s[62:63], v71, v68
	v_cmp_gt_u32_e64 s[66:67], v65, v68
	v_cmp_gt_u32_e64 s[78:79], v72, v68
	v_cmp_gt_u32_e64 s[82:83], v64, v68
	v_cmp_gt_u32_e64 s[92:93], v1, v68
	v_mov_b32_e32 v168, v124
	v_mov_b32_e32 v169, v124
	v_mov_b32_e32 v170, v124
	v_mov_b32_e32 v171, v124
	s_mov_b32 s28, 1
	v_readlane_b32 s94, v254, 50
	s_nop 0
	s_add_i32 s10, s94, -8
	v_mov_b32_e32 v65, s10
	ds_read_b32 v65, v65
	s_waitcnt lgkmcnt(0)
.LBB0_486:
	v_readfirstlane_b32 s12, v65
	s_ashr_i32 s95, s12, 8
	s_cmp_lg_u32 s95, s31
	s_cselect_b64 s[10:11], -1, 0
	s_cmp_eq_u32 s95, s31
	s_cbranch_scc1 .LBB0_488
	ds_bpermute_b32 v1, v172, v167
	s_mov_b32 s31, s95
	s_waitcnt lgkmcnt(0)
	v_add_f32_e32 v1, v167, v1
	v_div_scale_f32 v34, s[14:15], v1, v1, v181
	v_rcp_f32_e32 v35, v34
	v_div_scale_f32 v36, vcc, v181, v1, v181
	v_fma_f32 v37, -v34, v35, 1.0
	v_fmac_f32_e32 v35, v37, v35
	v_mul_f32_e32 v37, v36, v35
	v_fma_f32 v38, -v34, v37, v36
	v_fmac_f32_e32 v37, v38, v35
	v_fma_f32 v34, -v34, v37, v36
	v_div_fmas_f32 v34, v34, v35, v37
	v_div_fixup_f32 v34, v34, v1, v181
	v_pk_fma_f32 v[150:151], v[18:19], v[34:35], v[150:151] op_sel_hi:[1,0,1]
	v_mov_b32_e32 v18, 0
	v_pk_fma_f32 v[156:157], v[2:3], v[34:35], v[156:157] op_sel_hi:[1,0,1]
	v_pk_fma_f32 v[146:147], v[20:21], v[34:35], v[146:147] op_sel_hi:[1,0,1]
	v_pk_fma_f32 v[154:155], v[4:5], v[34:35], v[154:155] op_sel_hi:[1,0,1]
	v_pk_fma_f32 v[142:143], v[22:23], v[34:35], v[142:143] op_sel_hi:[1,0,1]
	v_pk_fma_f32 v[152:153], v[6:7], v[34:35], v[152:153] op_sel_hi:[1,0,1]
	v_pk_fma_f32 v[138:139], v[24:25], v[34:35], v[138:139] op_sel_hi:[1,0,1]
	v_pk_fma_f32 v[148:149], v[8:9], v[34:35], v[148:149] op_sel_hi:[1,0,1]
	v_pk_fma_f32 v[134:135], v[26:27], v[34:35], v[134:135] op_sel_hi:[1,0,1]
	v_pk_fma_f32 v[144:145], v[10:11], v[34:35], v[144:145] op_sel_hi:[1,0,1]
	v_pk_fma_f32 v[130:131], v[28:29], v[34:35], v[130:131] op_sel_hi:[1,0,1]
	v_pk_fma_f32 v[140:141], v[12:13], v[34:35], v[140:141] op_sel_hi:[1,0,1]
	v_pk_fma_f32 v[128:129], v[30:31], v[34:35], v[128:129] op_sel_hi:[1,0,1]
	v_pk_fma_f32 v[136:137], v[14:15], v[34:35], v[136:137] op_sel_hi:[1,0,1]
	v_pk_fma_f32 v[126:127], v[32:33], v[34:35], v[126:127] op_sel_hi:[1,0,1]
	v_pk_fma_f32 v[132:133], v[16:17], v[34:35], v[132:133] op_sel_hi:[1,0,1]
	v_mov_b32_e32 v19, v18
	v_mov_b32_e32 v20, v18
	v_mov_b32_e32 v21, v18
	v_mov_b32_e32 v22, v18
	v_mov_b32_e32 v23, v18
	v_mov_b32_e32 v24, v18
	v_mov_b32_e32 v25, v18
	v_mov_b32_e32 v26, v18
	v_mov_b32_e32 v27, v18
	v_mov_b32_e32 v28, v18
	v_mov_b32_e32 v29, v18
	v_mov_b32_e32 v30, v18
	v_mov_b32_e32 v31, v18
	v_mov_b32_e32 v32, v18
	v_mov_b32_e32 v33, v18
	v_mov_b32_e32 v2, v18
	v_mov_b32_e32 v3, v18
	v_mov_b32_e32 v4, v18
	v_mov_b32_e32 v5, v18
	v_mov_b32_e32 v6, v18
	v_mov_b32_e32 v7, v18
	v_mov_b32_e32 v8, v18
	v_mov_b32_e32 v9, v18
	v_mov_b32_e32 v10, v18
	v_mov_b32_e32 v11, v18
	v_mov_b32_e32 v12, v18
	v_mov_b32_e32 v13, v18
	v_mov_b32_e32 v14, v18
	v_mov_b32_e32 v15, v18
	v_mov_b32_e32 v16, v18
	v_mov_b32_e32 v17, v18
	v_mov_b32_e32 v166, v18
	v_mov_b32_e32 v167, v18

; #define LAS __attribute__((address_space(3)))
; #define MFMA32(a, b, c) __builtin_amdgcn_mfma_f32_32x32x16_bf16((a), (b), (c), 0, 0, 0)
; __device__ __forceinline__ void unit(LAS unsigned char* lds, const bf16* Z, const bf16* kct, const bf16* vct, bf16* OAp, int b, int g, int iq, const int tid_in) {
;     ...
; #pragma unroll
;             for (int d0 = 0; d0 < 4; ++d0) {
;                 const bf16x8 k0 = *(const LAS bf16x8*)(KSb[bi] + r32 * KST + 16 * d0 + 8 * hi);
;                 const bf16x8 k1 = *(const LAS bf16x8*)(KSb[bi] + (r32 + 32) * KST + 16 * d0 + 8 * hi);
;                 p0 = MFMA32(k0, qr[d0], p0); p1 = MFMA32(k1, qr[d0], p1); }
;             float mx = fmaxf(p0[0], p1[0]);
; #pragma unroll
;             for (int r = 1; r < 16; ++r) mx = fmaxf(mx, fmaxf(p0[r], p1[r]));
;             mx = fmaxf(mx, __shfl_xor(mx, 32));
.LBB0_496:
	s_bitcmp1_b32 s28, 0
	s_cselect_b32 s12, s37, 0
	v_add3_u32 v1, s12, v179, v180
	ds_read_b128 v[66:69], v1
	ds_read_b128 v[70:73], v1 offset:32
	s_andn2_b64 vcc, exec, s[10:11]
	s_mov_b64 s[10:11], -1
	s_waitcnt lgkmcnt(1)
	v_mfma_f32_32x32x16_bf16 v[34:49], v[66:69], v[98:101], v[34:49]
	ds_read_b128 v[66:69], v1 offset:4608
	ds_read_b128 v[74:77], v1 offset:4640
	s_waitcnt lgkmcnt(1)
	v_mfma_f32_32x32x16_bf16 v[50:65], v[66:69], v[98:101], v[50:65]
	v_mfma_f32_32x32x16_bf16 v[34:49], v[70:73], v[102:105], v[34:49]
	ds_read_b128 v[66:69], v1 offset:64
	ds_read_b128 v[70:73], v1 offset:96
	s_waitcnt lgkmcnt(2)
	v_mfma_f32_32x32x16_bf16 v[50:65], v[74:77], v[102:105], v[50:65]
	s_waitcnt lgkmcnt(1)
	v_mfma_f32_32x32x16_bf16 v[34:49], v[66:69], v[106:109], v[34:49]
	ds_read_b128 v[66:69], v1 offset:4672
	ds_read_b128 v[74:77], v1 offset:4704
	s_waitcnt lgkmcnt(1)
	v_mfma_f32_32x32x16_bf16 v[50:65], v[66:69], v[106:109], v[50:65]
	v_mfma_f32_32x32x16_bf16 v[34:49], v[70:73], v[110:113], v[34:49]
	s_waitcnt lgkmcnt(0)
	v_mfma_f32_32x32x16_bf16 v[50:65], v[74:77], v[110:113], v[50:65]
	s_nop 9
	v_max3_f32 v1, v34, v35, v36
	v_max3_f32 v66, v37, v38, v39
	v_max3_f32 v67, v50, v51, v52
	v_max3_f32 v68, v53, v54, v55
	v_max3_f32 v1, v1, v40, v41
	v_max3_f32 v66, v66, v42, v43
	v_max3_f32 v67, v67, v56, v57
	v_max3_f32 v68, v68, v58, v59
	v_max3_f32 v1, v1, v44, v45
	v_max3_f32 v66, v66, v46, v47
	v_max3_f32 v67, v67, v60, v61
	v_max3_f32 v68, v68, v62, v63
	v_max3_f32 v1, v1, v48, v49
	v_max3_f32 v67, v67, v64, v65
	v_max3_f32 v1, v1, v66, v67
	v_max_f32_e32 v1, v1, v68
	v_mov_b32_e32 v66, v1
	s_nop 1
	v_permlane32_swap_b32_e32 v66, v1
	v_max_f32_e32 v1, v66, v1
	s_cbranch_vccnz .LBB0_498
	s_mov_b32 s10, 0xff800000
	v_cmp_neq_f32_e32 vcc, s10, v1
	s_mov_b64 s[10:11], 0
	s_nop 0
	v_cndmask_b32_e32 v125, 0, v1, vcc
	v_sub_f32_e32 v81, v49, v125
	v_sub_f32_e32 v80, v48, v125
	v_sub_f32_e32 v79, v47, v125
	v_sub_f32_e32 v78, v46, v125
	v_sub_f32_e32 v77, v45, v125
	v_sub_f32_e32 v76, v44, v125
	v_sub_f32_e32 v75, v43, v125
	v_sub_f32_e32 v74, v42, v125
	v_sub_f32_e32 v73, v41, v125
	v_sub_f32_e32 v72, v40, v125
	v_sub_f32_e32 v71, v39, v125
	v_sub_f32_e32 v70, v38, v125
	v_sub_f32_e32 v69, v37, v125
	v_sub_f32_e32 v68, v36, v125
	v_sub_f32_e32 v67, v35, v125
	v_sub_f32_e32 v66, v34, v125
	v_sub_f32_e32 v97, v65, v125
	v_sub_f32_e32 v96, v64, v125
	v_sub_f32_e32 v95, v63, v125
	v_sub_f32_e32 v94, v62, v125
	v_sub_f32_e32 v93, v61, v125
	v_sub_f32_e32 v92, v60, v125
	v_sub_f32_e32 v91, v59, v125
	v_sub_f32_e32 v90, v58, v125
	v_sub_f32_e32 v89, v57, v125
	v_sub_f32_e32 v88, v56, v125
	v_sub_f32_e32 v87, v55, v125
	v_sub_f32_e32 v86, v54, v125
	v_sub_f32_e32 v85, v53, v125
	v_sub_f32_e32 v84, v52, v125
	v_sub_f32_e32 v83, v51, v125
	v_sub_f32_e32 v82, v50, v125
	v_add_f32_e32 v125, v166, v125

; #define LAS __attribute__((address_space(3)))
; __device__ __forceinline__ unsigned cvt_pk_bf16(float lo, float hi) { f32x2_t v = {lo, hi}; bf16x2_t b = __builtin_convertvector(v, bf16x2_t); return __builtin_bit_cast(unsigned, b); }
; #define MFMA32(a, b, c) __builtin_amdgcn_mfma_f32_32x32x16_bf16((a), (b), (c), 0, 0, 0)
; __device__ __forceinline__ void unit(LAS unsigned char* lds, const bf16* Z, const bf16* kct, const bf16* vct, bf16* OAp, int b, int g, int iq, const int tid_in) {
;     ...
;             float rs = 0.f;
; #pragma unroll
;             for (int r = 0; r < 16; ++r) { p0[r] = __builtin_amdgcn_exp2f(p0[r]); p1[r] = __builtin_amdgcn_exp2f(p1[r]); rs += p0[r] + p1[r]; }
;             l_run += rs;
; #pragma unroll
;             for (int s = 0; s < 4; ++s) {
;                 u32x4 pw;
;                 if (s < 2) { const int rb = 8 * s; pw.x = cvt_pk_bf16(p0[rb + 0], p0[rb + 1]); pw.y = cvt_pk_bf16(p0[rb + 2], p0[rb + 3]); pw.z = cvt_pk_bf16(p0[rb + 4], p0[rb + 5]); pw.w = cvt_pk_bf16(p0[rb + 6], p0[rb + 7]); }
;                 else { const int rb = 8 * (s - 2); pw.x = cvt_pk_bf16(p1[rb + 0], p1[rb + 1]); pw.y = cvt_pk_bf16(p1[rb + 2], p1[rb + 3]); pw.z = cvt_pk_bf16(p1[rb + 4], p1[rb + 5]); pw.w = cvt_pk_bf16(p1[rb + 6], p1[rb + 7]); }
;                 const bf16x8 pa = __builtin_bit_cast(bf16x8, pw);
; #pragma unroll
;                 for (int db = 0; db < 2; ++db) { const bf16x8 vf = *(const LAS bf16x8*)(VTb[bi] + (32 * db + r32) * KST + 16 * s + 8 * hi); o[db] = MFMA32(vf, pa, o[db]); } }
;             if (k + 1 < ntile) { NSA_STORE(bi ^ 1); if (k + 2 < ntile) NSA_LOAD(TL[3 + k]); }
;             asm volatile("s_waitcnt lgkmcnt(0)\n\ts_barrier" ::: "memory");
.LBB0_506:
	v_add_f32_e32 v1, v1, v34
	v_add_f32_e32 v34, v35, v36
	v_add_f32_e32 v1, 0, v1
	v_add_f32_e32 v35, v37, v38
	v_add_f32_e32 v1, v34, v1
	v_add_f32_e32 v36, v39, v40
	v_add_f32_e32 v1, v35, v1
	v_add_f32_e32 v37, v41, v42
	v_add_f32_e32 v1, v36, v1
	v_add_f32_e32 v38, v43, v44
	v_add_f32_e32 v1, v37, v1
	v_add_f32_e32 v39, v45, v46
	v_add_f32_e32 v1, v38, v1
	v_add_f32_e32 v40, v47, v48
	v_add_f32_e32 v1, v39, v1
	v_add_f32_e32 v41, v49, v50
	v_add_f32_e32 v1, v40, v1
	v_add_f32_e32 v42, v51, v52
	v_add_f32_e32 v1, v41, v1
	v_add_f32_e32 v43, v53, v54
	v_add_f32_e32 v1, v42, v1
	v_add_f32_e32 v44, v55, v56
	v_add_f32_e32 v1, v43, v1
	v_add_f32_e32 v45, v57, v58
	v_add_f32_e32 v1, v44, v1
	v_add_f32_e32 v46, v59, v60
	v_add_f32_e32 v1, v45, v1
	v_add_f32_e32 v47, v61, v62
	v_add_f32_e32 v1, v46, v1
	v_add_f32_e32 v48, v63, v64
	v_add_f32_e32 v1, v47, v1
	s_add_i32 s11, s94, -4
	v_mov_b32_e32 v65, s11
	ds_read_b32 v65, v65
	s_waitcnt lgkmcnt(0)
	s_barrier
	v_add_f32_e32 v1, v48, v1
	s_add_i32 s94, s94, 4
	v_add_f32_e32 v167, v167, v1
	s_cmp_lg_u32 s19, s10
	s_cbranch_scc0 .LBB0_411
	s_mov_b32 s28, s10
	s_branch .LBB0_486
